# MoE tile-list setup built by 64 lanes with coalesced loads instead of serial single-lane loop; dead per-XCD list removed
# speedup vs baseline: 1.5426x; 1.5426x over previous
; __global__ void __launch_bounds__(NWAVES * 64, 2) mk_fwd(Args args) {
;     ...
;         if (F.tid == 0) {
;             const int* te = WSP(int, WS_TILEE); int n = 0;
;             for (int e = xcd; e < NEXP; e += 8) { const int t0 = te[e], nt_ = te[128 + e]; for (int i = 0; i < nt_ && n < MAX_TILES; ++i) xlist[n++] = ((t0 + i) << 8) | e; }
;             { const int t0 = te[NEXP], per = (S_ / 256) / 8; for (int i = 0; i < per && n < MAX_TILES; ++i) xlist[n++] = ((t0 + xcd * per + i) << 8) | NEXP; }
;             xcnt[0] = n;
;         }
;         if (F.tid == 64) {
;             const int* te = WSP(int, WS_TILEE); int n = 0;
;             for (int e = 0; e < NE1; ++e) { const int t0 = te[e], nt_ = te[128 + e]; for (int i = 0; i < nt_ && n < MAX_TILES; ++i) flist[n++] = ((t0 + i) << 8) | e; }
;             xcnt[1] = n;
;         }
;         __syncthreads();
;         const int nfl = xcnt[1];
.LBB0_1553:
	s_andn2_b64 vcc, exec, s[4:5]
	s_cbranch_vccnz .LBB0_1708
	s_waitcnt vmcnt(0)
	v_mov_b32_e32 v1, v0
	s_mov_b64 s[4:5], s[0:1]
	s_load_dwordx2 s[8:9], s[4:5], 0xc8
	v_cmp_lt_i32_e32 vcc, 63, v1
	s_and_saveexec_b64 s[4:5], vcc
	s_xor_b64 s[4:5], exec, s[4:5]
	s_cbranch_execz .LBB0_1572
	v_lshrrev_b32_e32 v2, 6, v1
	v_cmp_eq_u32_e32 vcc, 1, v2
	s_and_saveexec_b64 s[6:7], vcc
	s_cbranch_execz .LBB0_1571
	s_waitcnt lgkmcnt(0)
	s_add_u32 s18, s8, 0x160000
	s_addc_u32 s19, s9, 0
	v_and_b32_e32 v1, 63, v1
	v_lshlrev_b32_e32 v2, 2, v1
	global_load_dword v3, v2, s[18:19]
	global_load_dword v4, v2, s[18:19] offset:512
	global_load_dword v5, v2, s[18:19] offset:256
	s_waitcnt vmcnt(0)
	v_lshlrev_b32_e32 v6, 2, v3
	v_readfirstlane_b32 s12, v5
	v_add_u32_e32 v6, 0x20e08, v6
	v_lshl_or_b32 v7, v3, 8, v1
.Lmy_fl_loop:
	v_cmp_lt_i32_e32 vcc, 0, v4
	s_cbranch_vccz .Lmy_fl_done
	s_and_saveexec_b64 s[14:15], vcc
	ds_write_b32 v6, v7
	s_mov_b64 exec, s[14:15]
	v_add_u32_e32 v6, 4, v6
	v_add_u32_e32 v7, 0x100, v7
	v_add_u32_e32 v4, -1, v4
	s_branch .Lmy_fl_loop
.Lmy_fl_done:
	v_add_u32_e32 v3, s12, v1
	v_lshlrev_b32_e32 v6, 2, v3
	v_add_u32_e32 v6, 0x20e08, v6
	v_lshl_or_b32 v7, v3, 8, 64
	ds_write_b32 v6, v7
	s_add_i32 s12, s12, 64
	v_mov_b32_e32 v1, 0x20204
	v_mov_b32_e32 v2, s12
	ds_write_b32 v1, v2

; __global__ void __launch_bounds__(NWAVES * 64, 2) mk_fwd(Args args) {
;     ...
;         if (F.tid == 0) {
;             const int* te = WSP(int, WS_TILEE); int n = 0;
;             for (int e = xcd; e < NEXP; e += 8) { const int t0 = te[e], nt_ = te[128 + e]; for (int i = 0; i < nt_ && n < MAX_TILES; ++i) xlist[n++] = ((t0 + i) << 8) | e; }
;             { const int t0 = te[NEXP], per = (S_ / 256) / 8; for (int i = 0; i < per && n < MAX_TILES; ++i) xlist[n++] = ((t0 + xcd * per + i) << 8) | NEXP; }
;             xcnt[0] = n;
;         }
.LBB0_1572:
	s_or_saveexec_b64 s[4:5], s[4:5]
	s_and_b32 s64, s2, 7
	s_xor_b64 exec, exec, s[4:5]
	s_cbranch_execz .LBB0_1607
	s_mov_b32 s13, 0
	v_cmp_eq_u32_e32 vcc, 0, v1
	s_and_saveexec_b64 s[6:7], vcc
	s_branch .LBB0_1606
